# v12 + shared-expert weight conversion jobs of the prologue moved to the 64 workgroups that have no adaLN GEMV job
# speedup vs baseline: 1.0353x; 1.0353x over previous
; __device__ __forceinline__ int tid_fresh() { int t = threadIdx.x; asm volatile("" : "+v"(t)); return t; }
; __device__ __forceinline__ KP kparams() { KP q = (KP)__builtin_amdgcn_kernarg_segment_ptr(); asm volatile("" : "+s"(q)); return q; }
; #define CVT_LOAD(jx) do { const int b_ = (jx) / per, r_ = (jx) - b_ * per, kt_ = r_ / tn, nt_ = r_ - kt_ * tn; \
;         const float* s_ = src + (size_t)b_ * sbs + (size_t)(kt_ * 64) * ldS + nt_ * 256; \
;         _Pragma("unroll") for (int q = 0; q < 8; ++q) v[q] = *(const float4*)(s_ + (size_t)(kr + 8 * q) * ldS + c4 * 4); } while (0)
;     const int tid = tid_fresh();
;     const int tk = K / 64, tn = N / 256, per = tk * tn, total = per * nbatch;
;     const int kr = tid >> 6, c4 = tid & 63;
;     ...
;     float4 v[8];
;     if (bid < total) CVT_LOAD(bid);
;     for (int j = bid; j < total; j += G) {
;         const int b = j / per, r = j - b * per, kt = r / tn, ntile = r - kt * tn;
; __global__ void __launch_bounds__(NTHR, 2) fwd(Params p_unused) {
;     ...
;         for (int l2 = 0; l2 < 2 * REP_CVT; ++l2) { const int l = l2 & 1;
;             KP kp = kparams(); bf16_t* Wgu = (bf16_t*)(kp->ws + WS_WGU) + l * WGU_L; bf16_t* Wd = (bf16_t*)(kp->ws + WS_WD) + l * WD_L;
;             cvt_group(tile, bid, G, kp->in[30] + (size_t)l * D * FF, 0, FF, D, FF, Wgu + (size_t)NE * 1024 * D, 0, 1, 1, 1024);
;             cvt_group(tile, bid, G, kp->in[31] + (size_t)l * D * FF, 0, FF, D, FF, Wgu + (size_t)NE * 1024 * D, 0, 2, 1, 1024);
;             cvt_group(tile, bid, G, kp->in[32] + (size_t)l * FF * D, 0, D, FF, D, Wd + (size_t)NE * D * FF, 0, 0, 1, D);
.LBB0_112:
	v_readlane_b32 s4, v254, 19
	s_add_u32 s4, s4, 64
	s_and_b32 s4, s4, 0xff
	v_readlane_b32 s5, v254, 20
	s_cmp_lt_i32 s4, 64
	s_cselect_b64 s[0:1], -1, 0
	s_lshr_b32 s2, s5, 26
	s_add_i32 s2, s4, s2
	s_andn2_b32 s2, s2, 63
	s_sub_i32 s4, s4, s2
	s_bfe_i32 s5, s4, 0x80000
	s_bfe_u32 s2, s4, 0x10007
	s_bfe_u32 s5, s5, 0x3000c
	s_add_i32 s2, s4, s2
	s_lshl_b32 s8, s4, 8
	s_add_i32 s4, s4, s5
	s_bfe_i32 s2, s2, 0x80000
	s_bfe_i32 s4, s4, 0x80000
	s_sext_i32_i16 s2, s2
	s_sext_i32_i16 s4, s4
	s_ashr_i32 s6, s2, 1
	s_ashr_i32 s9, s4, 3
	s_lshl_b32 s2, s6, 6
	s_lshl_b32 s6, s6, 9
	s_lshl_b32 s4, s9, 6
	s_lshl_b32 s9, s9, 11
	s_sub_i32 s6, s8, s6
	s_sub_i32 s10, s8, s9
	s_ashr_i32 s3, s2, 31
	s_ashr_i32 s7, s6, 31
	s_ashr_i32 s5, s4, 31
	s_ashr_i32 s11, s10, 31
	v_cndmask_b32_e64 v1, 0, 1, s[0:1]
	s_lshl_b64 s[2:3], s[2:3], 11
	s_lshl_b64 s[4:5], s[4:5], 13
	s_mov_b64 s[14:15], 0
	s_mov_b64 s[8:9], -1
	v_cmp_ne_u32_e64 s[0:1], 1, v1
	s_lshl_b64 s[6:7], s[6:7], 2
	v_mov_b32_e32 v35, 0
	s_movk_i32 s13, 0x2020
	s_movk_i32 s17, 0x404
	s_movk_i32 s26, 0xff00
	s_lshl_b64 s[10:11], s[10:11], 2
	s_barrier
	s_branch .LBB0_114

; #define LAS __attribute__((address_space(3)))
; __device__ __forceinline__ int tid_fresh() { int t = threadIdx.x; asm volatile("" : "+v"(t)); return t; }
; #define CVT_LOAD(jx) do { const int b_ = (jx) / per, r_ = (jx) - b_ * per, kt_ = r_ / tn, nt_ = r_ - kt_ * tn; \
;         const float* s_ = src + (size_t)b_ * sbs + (size_t)(kt_ * 64) * ldS + nt_ * 256; \
;         _Pragma("unroll") for (int q = 0; q < 8; ++q) v[q] = *(const float4*)(s_ + (size_t)(kr + 8 * q) * ldS + c4 * 4); } while (0)
;     const int tid = tid_fresh();
;     const int tk = K / 64, tn = N / 256, per = tk * tn, total = per * nbatch;
;     const int kr = tid >> 6, c4 = tid & 63;
;     ...
;     float4 v[8];
;     if (bid < total) CVT_LOAD(bid);
;     for (int j = bid; j < total; j += G) {
;         const int b = j / per, r = j - b * per, kt = r / tn, ntile = r - kt * tn;
;         __syncthreads();
; #pragma unroll
;         for (int q = 0; q < 8; ++q) { LAS float* tp = tile + (kr + 8 * q) * 257 + c4 * 4; tp[0] = v[q].x; tp[1] = v[q].y; tp[2] = v[q].z; tp[3] = v[q].w; }
;         if (j + G < total) CVT_LOAD(j + G);
;         __syncthreads();
;         bf16_t* dmat = dst + (size_t)b * dbs;
; #pragma unroll
;         for (int q = 0; q < 4; ++q) {
;             const int id = tid + NTHR * q, nr = id >> 3, kc = id & 7;
.LBB0_114:
	v_readlane_b32 s18, v254, 0
	v_readlane_b32 s19, v254, 1
	s_load_dwordx2 s[20:21], s[18:19], 0x118
	s_mul_i32 s22, s14, 0x10400000
	v_mov_b32_e32 v61, v0
	s_waitcnt lgkmcnt(0)
	s_add_u32 s27, s20, s22
	s_addc_u32 s28, s21, 0
	s_lshl_b64 s[22:23], s[14:15], 20
	s_add_u32 s20, s27, 0x14030000
	s_addc_u32 s21, s28, 0
	s_and_b64 vcc, exec, s[0:1]
	s_cbranch_vccnz .LBB0_119
	s_load_dwordx2 s[24:25], s[18:19], 0xf0
	s_lshl_b64 s[30:31], s[22:23], 2
	v_and_b32_e32 v1, 63, v61
	v_ashrrev_i32_e32 v52, 6, v61
	v_lshlrev_b32_e32 v34, 4, v1
	s_waitcnt lgkmcnt(0)
	s_add_u32 s29, s24, s30
	s_addc_u32 s30, s25, s31
	s_add_u32 s24, s29, s2
	s_addc_u32 s25, s30, s3
	s_add_u32 s24, s24, s6
	s_addc_u32 s25, s25, s7
	v_ashrrev_i32_e32 v53, 31, v52
	v_add_u32_e32 v38, 8, v52
	s_waitcnt vmcnt(5)
	v_lshl_add_u64 v[26:27], s[24:25], 0, v[34:35]
	v_lshlrev_b64 v[2:3], 11, v[52:53]
	v_ashrrev_i32_e32 v39, 31, v38
	v_add_u32_e32 v40, 16, v52
	v_lshl_add_u64 v[10:11], v[26:27], 0, v[2:3]
	v_lshlrev_b64 v[2:3], 11, v[38:39]
	v_ashrrev_i32_e32 v41, 31, v40
	v_add_u32_e32 v42, 24, v52
	v_lshl_add_u64 v[12:13], v[26:27], 0, v[2:3]
	global_load_dwordx4 v[2:5], v[10:11], off nt
	global_load_dwordx4 v[6:9], v[12:13], off nt
	v_lshlrev_b64 v[10:11], 11, v[40:41]
	v_ashrrev_i32_e32 v43, 31, v42
	v_add_u32_e32 v44, 32, v52
	v_lshl_add_u64 v[18:19], v[26:27], 0, v[10:11]
	v_lshlrev_b64 v[10:11], 11, v[42:43]
	v_ashrrev_i32_e32 v45, 31, v44
	v_add_u32_e32 v46, 40, v52
	v_lshl_add_u64 v[20:21], v[26:27], 0, v[10:11]
	global_load_dwordx4 v[10:13], v[18:19], off nt
	global_load_dwordx4 v[14:17], v[20:21], off nt
	v_lshlrev_b64 v[18:19], 11, v[44:45]
	v_ashrrev_i32_e32 v47, 31, v46
	v_add_u32_e32 v48, 48, v52
	v_lshl_add_u64 v[28:29], v[26:27], 0, v[18:19]
	v_lshlrev_b64 v[18:19], 11, v[46:47]
	v_ashrrev_i32_e32 v49, 31, v48
	v_add_u32_e32 v50, 56, v52
	s_waitcnt vmcnt(8)
	v_lshl_add_u64 v[30:31], v[26:27], 0, v[18:19]
	global_load_dwordx4 v[18:21], v[28:29], off nt
	global_load_dwordx4 v[22:25], v[30:31], off nt
	v_lshlrev_b64 v[28:29], 11, v[48:49]
	v_ashrrev_i32_e32 v51, 31, v50
	v_lshl_add_u64 v[36:37], v[26:27], 0, v[28:29]
	v_lshlrev_b64 v[28:29], 11, v[50:51]
	v_lshl_add_u64 v[54:55], v[26:27], 0, v[28:29]
	global_load_dwordx4 v[26:29], v[36:37], off nt
	global_load_dwordx4 v[30:33], v[54:55], off nt
	v_lshlrev_b32_e32 v66, 2, v1
	v_lshlrev_b64 v[36:37], 9, v[52:53]
	v_and_b32_e32 v1, 7, v61
	v_mul_lo_u32 v64, v52, s17
	v_ashrrev_i32_e32 v52, 3, v61
	v_add_u32_e32 v55, 0x200, v61
	v_add_u32_e32 v58, 0x400, v61
	v_add_u32_e32 v61, 0x600, v61
	v_add_u32_e32 v34, 0, v34
	v_mad_u32_u24 v63, v1, s13, 0
	v_ashrrev_i32_e32 v55, 3, v55
	v_ashrrev_i32_e32 v58, 3, v58
	v_ashrrev_i32_e32 v61, 3, v61
	v_readlane_b32 s24, v254, 19
	s_add_u32 s24, s24, 64
	s_and_b32 s24, s24, 0xff
	v_lshlrev_b64 v[38:39], 9, v[38:39]
	v_lshlrev_b64 v[40:41], 9, v[40:41]
	v_lshlrev_b64 v[42:43], 9, v[42:43]
	v_lshlrev_b64 v[44:45], 9, v[44:45]
	v_lshlrev_b64 v[46:47], 9, v[46:47]
	v_lshlrev_b64 v[48:49], 9, v[48:49]
	v_lshlrev_b64 v[50:51], 9, v[50:51]
	v_and_b32_e32 v53, 0x7f, v52
	v_lshl_add_u32 v54, v52, 2, v63
	v_and_b32_e32 v56, 0x7f, v55
	v_lshl_add_u32 v57, v55, 2, v63
	v_and_b32_e32 v59, 0x7f, v58
	v_lshl_add_u32 v60, v58, 2, v63
	v_and_b32_e32 v62, 0x7f, v61
	v_lshl_add_u32 v63, v61, 2, v63
	v_add_u32_e32 v64, v34, v64
	v_lshlrev_b32_e32 v34, 2, v66
	s_mov_b32 s33, s24
	v_readlane_b32 s25, v254, 20
	s_branch .LBB0_117

; #define LAS __attribute__((address_space(3)))
; __device__ __forceinline__ int tid_fresh() { int t = threadIdx.x; asm volatile("" : "+v"(t)); return t; }
; __device__ __forceinline__ KP kparams() { KP q = (KP)__builtin_amdgcn_kernarg_segment_ptr(); asm volatile("" : "+s"(q)); return q; }
; #define CVT_LOAD(jx) do { const int b_ = (jx) / per, r_ = (jx) - b_ * per, kt_ = r_ / tn, nt_ = r_ - kt_ * tn; \
;         const float* s_ = src + (size_t)b_ * sbs + (size_t)(kt_ * 64) * ldS + nt_ * 256; \
;         _Pragma("unroll") for (int q = 0; q < 8; ++q) v[q] = *(const float4*)(s_ + (size_t)(kr + 8 * q) * ldS + c4 * 4); } while (0)
;     const int tid = tid_fresh();
;     const int tk = K / 64, tn = N / 256, per = tk * tn, total = per * nbatch;
;     const int kr = tid >> 6, c4 = tid & 63;
;     ...
;     float4 v[8];
;     if (bid < total) CVT_LOAD(bid);
;     for (int j = bid; j < total; j += G) {
;         const int b = j / per, r = j - b * per, kt = r / tn, ntile = r - kt * tn;
;         __syncthreads();
; #pragma unroll
;         for (int q = 0; q < 8; ++q) { LAS float* tp = tile + (kr + 8 * q) * 257 + c4 * 4; tp[0] = v[q].x; tp[1] = v[q].y; tp[2] = v[q].z; tp[3] = v[q].w; }
;         if (j + G < total) CVT_LOAD(j + G);
;         __syncthreads();
;         bf16_t* dmat = dst + (size_t)b * dbs;
; #pragma unroll
;         for (int q = 0; q < 4; ++q) {
;             const int id = tid + NTHR * q, nr = id >> 3, kc = id & 7;
; __global__ void __launch_bounds__(NTHR, 2) fwd(Params p_unused) {
;     ...
;         for (int l2 = 0; l2 < 2 * REP_CVT; ++l2) { const int l = l2 & 1;
;             KP kp = kparams(); bf16_t* Wgu = (bf16_t*)(kp->ws + WS_WGU) + l * WGU_L; bf16_t* Wd = (bf16_t*)(kp->ws + WS_WD) + l * WD_L;
;             cvt_group(tile, bid, G, kp->in[30] + (size_t)l * D * FF, 0, FF, D, FF, Wgu + (size_t)NE * 1024 * D, 0, 1, 1, 1024);
;             cvt_group(tile, bid, G, kp->in[31] + (size_t)l * D * FF, 0, FF, D, FF, Wgu + (size_t)NE * 1024 * D, 0, 2, 1, 1024);
;             cvt_group(tile, bid, G, kp->in[32] + (size_t)l * FF * D, 0, D, FF, D, Wd + (size_t)NE * D * FF, 0, 0, 1, D);
.LBB0_119:
	v_mov_b32_e32 v58, v0
	s_and_b64 vcc, exec, s[0:1]
	s_barrier
	s_cbranch_vccnz .LBB0_124
	s_load_dwordx2 s[24:25], s[18:19], 0xf8
	s_lshl_b64 s[22:23], s[22:23], 2
	v_and_b32_e32 v1, 63, v58
	v_ashrrev_i32_e32 v52, 6, v58
	v_lshlrev_b32_e32 v34, 4, v1
	s_waitcnt lgkmcnt(0)
	s_add_u32 s24, s24, s22
	s_addc_u32 s25, s25, s23
	s_add_u32 s22, s24, s2
	s_addc_u32 s23, s25, s3
	s_add_u32 s22, s22, s6
	s_addc_u32 s23, s23, s7
	v_ashrrev_i32_e32 v53, 31, v52
	v_add_u32_e32 v38, 8, v52
	s_waitcnt vmcnt(5)
	v_lshl_add_u64 v[26:27], s[22:23], 0, v[34:35]
	v_lshlrev_b64 v[2:3], 11, v[52:53]
	v_ashrrev_i32_e32 v39, 31, v38
	v_add_u32_e32 v40, 16, v52
	v_lshl_add_u64 v[10:11], v[26:27], 0, v[2:3]
	v_lshlrev_b64 v[2:3], 11, v[38:39]
	v_ashrrev_i32_e32 v41, 31, v40
	v_add_u32_e32 v42, 24, v52
	v_lshl_add_u64 v[12:13], v[26:27], 0, v[2:3]
	global_load_dwordx4 v[2:5], v[10:11], off nt
	global_load_dwordx4 v[6:9], v[12:13], off nt
	v_lshlrev_b64 v[10:11], 11, v[40:41]
	v_ashrrev_i32_e32 v43, 31, v42
	v_add_u32_e32 v44, 32, v52
	v_lshl_add_u64 v[18:19], v[26:27], 0, v[10:11]
	v_lshlrev_b64 v[10:11], 11, v[42:43]
	v_ashrrev_i32_e32 v45, 31, v44
	v_add_u32_e32 v46, 40, v52
	v_lshl_add_u64 v[20:21], v[26:27], 0, v[10:11]
	global_load_dwordx4 v[10:13], v[18:19], off nt
	global_load_dwordx4 v[14:17], v[20:21], off nt
	v_lshlrev_b64 v[18:19], 11, v[44:45]
	v_ashrrev_i32_e32 v47, 31, v46
	v_add_u32_e32 v48, 48, v52
	v_lshl_add_u64 v[28:29], v[26:27], 0, v[18:19]
	v_lshlrev_b64 v[18:19], 11, v[46:47]
	v_ashrrev_i32_e32 v49, 31, v48
	v_add_u32_e32 v50, 56, v52
	s_waitcnt vmcnt(8)
	v_lshl_add_u64 v[30:31], v[26:27], 0, v[18:19]
	global_load_dwordx4 v[18:21], v[28:29], off nt
	global_load_dwordx4 v[22:25], v[30:31], off nt
	v_lshlrev_b64 v[28:29], 11, v[48:49]
	v_ashrrev_i32_e32 v51, 31, v50
	v_lshl_add_u64 v[36:37], v[26:27], 0, v[28:29]
	v_lshlrev_b64 v[28:29], 11, v[50:51]
	v_lshl_add_u64 v[54:55], v[26:27], 0, v[28:29]
	global_load_dwordx4 v[26:29], v[36:37], off nt
	global_load_dwordx4 v[30:33], v[54:55], off nt
	v_lshlrev_b32_e32 v66, 2, v1
	v_lshlrev_b64 v[36:37], 9, v[52:53]
	v_and_b32_e32 v1, 7, v58
	v_mul_lo_u32 v64, v52, s17
	v_ashrrev_i32_e32 v52, 3, v58
	v_add_u32_e32 v54, 0x200, v58
	v_add_u32_e32 v56, 0x400, v58
	v_add_u32_e32 v58, 0x600, v58
	v_ashrrev_i32_e32 v54, 3, v54
	v_ashrrev_i32_e32 v56, 3, v56
	v_ashrrev_i32_e32 v58, 3, v58
	v_add_u32_e32 v34, 0, v34
	v_mad_u32_u24 v59, v1, s13, 0
	v_and_b32_e32 v60, 0x7f, v52
	v_and_b32_e32 v61, 0x7f, v54
	v_and_b32_e32 v62, 0x7f, v56
	v_and_b32_e32 v63, 0x7f, v58
	v_readlane_b32 s22, v254, 19
	s_add_u32 s22, s22, 64
	s_and_b32 s22, s22, 0xff
	v_lshlrev_b64 v[38:39], 9, v[38:39]
	v_lshlrev_b64 v[40:41], 9, v[40:41]
	v_lshlrev_b64 v[42:43], 9, v[42:43]
	v_lshlrev_b64 v[44:45], 9, v[44:45]
	v_lshlrev_b64 v[46:47], 9, v[46:47]
	v_lshlrev_b64 v[48:49], 9, v[48:49]
	v_lshlrev_b64 v[50:51], 9, v[50:51]
	v_lshl_add_u32 v53, v52, 2, v59
	v_lshl_add_u32 v55, v54, 2, v59
	v_lshl_add_u32 v57, v56, 2, v59
	v_lshl_add_u32 v59, v58, 2, v59
	v_or_b32_e32 v60, 0x80, v60
	v_or_b32_e32 v61, 0x80, v61
	v_or_b32_e32 v62, 0x80, v62
	v_or_b32_e32 v63, 0x80, v63
	v_add_u32_e32 v64, v34, v64
	v_lshlrev_b32_e32 v34, 2, v66
	s_mov_b32 s30, s22
	v_readlane_b32 s23, v254, 20
	s_branch .LBB0_122

; #define LAS __attribute__((address_space(3)))
; __device__ __forceinline__ int tid_fresh() { int t = threadIdx.x; asm volatile("" : "+v"(t)); return t; }
; __device__ __forceinline__ KP kparams() { KP q = (KP)__builtin_amdgcn_kernarg_segment_ptr(); asm volatile("" : "+s"(q)); return q; }
; #define CVT_LOAD(jx) do { const int b_ = (jx) / per, r_ = (jx) - b_ * per, kt_ = r_ / tn, nt_ = r_ - kt_ * tn; \
;         const float* s_ = src + (size_t)b_ * sbs + (size_t)(kt_ * 64) * ldS + nt_ * 256; \
;         _Pragma("unroll") for (int q = 0; q < 8; ++q) v[q] = *(const float4*)(s_ + (size_t)(kr + 8 * q) * ldS + c4 * 4); } while (0)
;     const int tid = tid_fresh();
;     const int tk = K / 64, tn = N / 256, per = tk * tn, total = per * nbatch;
;     const int kr = tid >> 6, c4 = tid & 63;
;     ...
;     float4 v[8];
;     if (bid < total) CVT_LOAD(bid);
;     for (int j = bid; j < total; j += G) {
;         const int b = j / per, r = j - b * per, kt = r / tn, ntile = r - kt * tn;
;         __syncthreads();
; #pragma unroll
;         for (int q = 0; q < 8; ++q) { LAS float* tp = tile + (kr + 8 * q) * 257 + c4 * 4; tp[0] = v[q].x; tp[1] = v[q].y; tp[2] = v[q].z; tp[3] = v[q].w; }
;         if (j + G < total) CVT_LOAD(j + G);
;         __syncthreads();
;         bf16_t* dmat = dst + (size_t)b * dbs;
; #pragma unroll
;         for (int q = 0; q < 4; ++q) {
;             const int id = tid + NTHR * q, nr = id >> 3, kc = id & 7;
; __global__ void __launch_bounds__(NTHR, 2) fwd(Params p_unused) {
;     ...
;         for (int l2 = 0; l2 < 2 * REP_CVT; ++l2) { const int l = l2 & 1;
;             KP kp = kparams(); bf16_t* Wgu = (bf16_t*)(kp->ws + WS_WGU) + l * WGU_L; bf16_t* Wd = (bf16_t*)(kp->ws + WS_WD) + l * WD_L;
;             cvt_group(tile, bid, G, kp->in[30] + (size_t)l * D * FF, 0, FF, D, FF, Wgu + (size_t)NE * 1024 * D, 0, 1, 1, 1024);
;             cvt_group(tile, bid, G, kp->in[31] + (size_t)l * D * FF, 0, FF, D, FF, Wgu + (size_t)NE * 1024 * D, 0, 2, 1, 1024);
;             cvt_group(tile, bid, G, kp->in[32] + (size_t)l * FF * D, 0, D, FF, D, Wd + (size_t)NE * D * FF, 0, 0, 1, D);
.LBB0_124:
	v_mov_b32_e32 v58, v0
	s_and_b64 vcc, exec, s[0:1]
	s_barrier
	s_cbranch_vccnz .LBB0_113
	s_mul_hi_u32 s21, s14, 0xf7e00000
	s_load_dwordx2 s[18:19], s[18:19], 0x100
	s_mul_i32 s20, s15, 0xf7e00000
	s_sub_i32 s21, s21, s14
	s_add_i32 s21, s21, s20
	s_mul_i32 s20, s14, 0xf7e00000
	s_add_u32 s22, s27, s20
	s_addc_u32 s23, s28, s21
	s_lshl_b64 s[14:15], s[14:15], 22
	s_waitcnt lgkmcnt(0)
	s_add_u32 s20, s18, s14
	s_addc_u32 s21, s19, s15
	s_add_u32 s14, s22, 0x2c830000
	s_addc_u32 s15, s23, 0
	s_add_u32 s18, s20, s4
	s_addc_u32 s19, s21, s5
	v_and_b32_e32 v1, 63, v58
	v_ashrrev_i32_e32 v52, 6, v58
	s_add_u32 s18, s18, s10
	s_addc_u32 s19, s19, s11
	v_lshlrev_b32_e32 v34, 4, v1
	v_ashrrev_i32_e32 v53, 31, v52
	v_add_u32_e32 v38, 8, v52
	s_waitcnt vmcnt(5)
	v_lshl_add_u64 v[26:27], s[18:19], 0, v[34:35]
	v_lshlrev_b64 v[2:3], 13, v[52:53]
	v_ashrrev_i32_e32 v39, 31, v38
	v_add_u32_e32 v40, 16, v52
	v_lshl_add_u64 v[10:11], v[26:27], 0, v[2:3]
	v_lshlrev_b64 v[2:3], 13, v[38:39]
	v_ashrrev_i32_e32 v41, 31, v40
	v_add_u32_e32 v42, 24, v52
	v_lshl_add_u64 v[12:13], v[26:27], 0, v[2:3]
	global_load_dwordx4 v[2:5], v[10:11], off nt
	global_load_dwordx4 v[6:9], v[12:13], off nt
	v_lshlrev_b64 v[10:11], 13, v[40:41]
	v_ashrrev_i32_e32 v43, 31, v42
	v_add_u32_e32 v44, 32, v52
	v_lshl_add_u64 v[18:19], v[26:27], 0, v[10:11]
	v_lshlrev_b64 v[10:11], 13, v[42:43]
	v_ashrrev_i32_e32 v45, 31, v44
	v_add_u32_e32 v46, 40, v52
	v_lshl_add_u64 v[20:21], v[26:27], 0, v[10:11]
	global_load_dwordx4 v[10:13], v[18:19], off nt
	global_load_dwordx4 v[14:17], v[20:21], off nt
	v_lshlrev_b64 v[18:19], 13, v[44:45]
	v_ashrrev_i32_e32 v47, 31, v46
	v_add_u32_e32 v48, 48, v52
	v_lshl_add_u64 v[28:29], v[26:27], 0, v[18:19]
	v_lshlrev_b64 v[18:19], 13, v[46:47]
	v_ashrrev_i32_e32 v49, 31, v48
	v_add_u32_e32 v50, 56, v52
	s_waitcnt vmcnt(8)
	v_lshl_add_u64 v[30:31], v[26:27], 0, v[18:19]
	global_load_dwordx4 v[18:21], v[28:29], off nt
	global_load_dwordx4 v[22:25], v[30:31], off nt
	v_lshlrev_b64 v[28:29], 13, v[48:49]
	v_ashrrev_i32_e32 v51, 31, v50
	v_lshl_add_u64 v[36:37], v[26:27], 0, v[28:29]
	v_lshlrev_b64 v[28:29], 13, v[50:51]
	v_lshl_add_u64 v[54:55], v[26:27], 0, v[28:29]
	global_load_dwordx4 v[26:29], v[36:37], off nt
	global_load_dwordx4 v[30:33], v[54:55], off nt
	v_lshlrev_b32_e32 v62, 2, v1
	v_lshlrev_b64 v[36:37], 11, v[52:53]
	v_and_b32_e32 v1, 7, v58
	v_mul_lo_u32 v60, v52, s17
	v_ashrrev_i32_e32 v52, 3, v58
	v_add_u32_e32 v54, 0x200, v58
	v_add_u32_e32 v56, 0x400, v58
	v_add_u32_e32 v58, 0x600, v58
	v_add_u32_e32 v34, 0, v34
	v_mad_u32_u24 v59, v1, s13, 0
	v_ashrrev_i32_e32 v54, 3, v54
	v_ashrrev_i32_e32 v56, 3, v56
	v_ashrrev_i32_e32 v58, 3, v58
	v_readlane_b32 s18, v254, 19
	s_add_u32 s18, s18, 64
	s_and_b32 s18, s18, 0xff
	v_lshlrev_b64 v[38:39], 11, v[38:39]
	v_lshlrev_b64 v[40:41], 11, v[40:41]
	v_lshlrev_b64 v[42:43], 11, v[42:43]
	v_lshlrev_b64 v[44:45], 11, v[44:45]
	v_lshlrev_b64 v[46:47], 11, v[46:47]
	v_lshlrev_b64 v[48:49], 11, v[48:49]
	v_lshlrev_b64 v[50:51], 11, v[50:51]
	v_lshl_add_u32 v53, v52, 2, v59
	v_lshl_add_u32 v55, v54, 2, v59
	v_lshl_add_u32 v57, v56, 2, v59
	v_lshl_add_u32 v59, v58, 2, v59
	v_add_u32_e32 v60, v34, v60
	v_lshlrev_b32_e32 v34, 2, v62
	s_mov_b32 s23, s18
	v_readlane_b32 s19, v254, 20
	s_branch .LBB0_127
